# P6/P7 epilogue: MFMA->VALU s_nop pad dropped (covered by >=25 instructions + bias wait), on top of v72
# baseline (speedup 1.0000x reference)
.LBB0_783:
	s_waitcnt vmcnt(0)
	v_pk_mul_f32 v[8:9], v[6:7], s[20:21] op_sel_hi:[1,0]
	v_pk_mul_f32 v[10:11], v[4:5], s[20:21] op_sel_hi:[1,0]
	v_pk_mul_f32 v[6:7], v[12:13], s[20:21] op_sel_hi:[1,0]
	v_pk_mul_f32 v[4:5], v[14:15], s[20:21] op_sel_hi:[1,0]
	v_pk_fma_f32 v[158:159], v[158:159], s[22:23], v[10:11] op_sel_hi:[1,0,1]
	v_pk_fma_f32 v[154:155], v[154:155], s[22:23], v[6:7] op_sel_hi:[1,0,1]
	v_pk_fma_f32 v[156:157], v[156:157], s[22:23], v[4:5] op_sel_hi:[1,0,1]
	v_pk_add_f32 v[16:17], v[26:27], 1.0 op_sel_hi:[1,0]
	v_pk_add_f32 v[18:19], v[24:25], 1.0 op_sel_hi:[1,0]
	v_min_f32_e32 v24, 0x42600000, v158
	v_min_f32_e32 v26, 0x42600000, v154
	v_min_f32_e32 v25, 0x42600000, v159
	v_min_f32_e32 v27, 0x42600000, v155
	v_pk_add_f32 v[12:13], v[30:31], 1.0 op_sel_hi:[1,0]
	v_min_f32_e32 v31, 0x42600000, v157
	v_mul_f32_e32 v23, 0xbe9d265f, v24
	v_mul_f32_e32 v155, 0xbe9d265f, v26
	v_mul_f32_e32 v157, 0xbe9d265f, v25
	v_mul_f32_e32 v158, 0xbe9d265f, v27
	v_min_f32_e32 v30, 0x42600000, v156
	v_exp_f32_e32 v154, v23
	v_exp_f32_e32 v156, v155
	v_exp_f32_e32 v155, v157
	v_exp_f32_e32 v157, v158
	v_pk_fma_f32 v[160:161], v[160:161], s[22:23], v[8:9] op_sel_hi:[1,0,1]
	v_pk_add_f32 v[14:15], v[28:29], 1.0 op_sel_hi:[1,0]
	v_min_f32_e32 v28, 0x42600000, v160
	v_min_f32_e32 v29, 0x42600000, v161
	v_pk_fma_f32 v[144:145], v[144:145], s[24:25], v[16:17] op_sel_hi:[1,0,1]
	v_pk_fma_f32 v[140:141], v[140:141], s[24:25], v[12:13] op_sel_hi:[1,0,1]
	v_mul_f32_e32 v159, 0xbe9d265f, v28
	v_mul_f32_e32 v160, 0xbe9d265f, v30
	v_mul_f32_e32 v161, 0xbe9d265f, v29
	v_mul_f32_e32 v171, 0xbe9d265f, v31
	v_med3_f32 v144, v144, s76, v213
	v_med3_f32 v140, v140, s76, v213
	v_med3_f32 v145, v145, s76, v213
	v_med3_f32 v141, v141, s76, v213
	v_exp_f32_e32 v158, v159
	v_exp_f32_e32 v160, v160
	v_exp_f32_e32 v159, v161
	v_exp_f32_e32 v161, v171
	v_pk_mul_f32 v[28:29], v[28:29], v[144:145]
	v_pk_mul_f32 v[30:31], v[30:31], v[140:141]
	v_pk_add_f32 v[140:141], v[154:155], 1.0 op_sel_hi:[1,0]
	v_pk_add_f32 v[144:145], v[156:157], 1.0 op_sel_hi:[1,0]
	v_rcp_f32_e32 v140, v140
	v_rcp_f32_e32 v144, v144
	v_rcp_f32_e32 v141, v141
	v_rcp_f32_e32 v145, v145
	v_pk_fma_f32 v[142:143], v[142:143], s[24:25], v[18:19] op_sel_hi:[1,0,1]
	v_pk_fma_f32 v[138:139], v[138:139], s[24:25], v[14:15] op_sel_hi:[1,0,1]
	v_med3_f32 v142, v142, s76, v213
	v_med3_f32 v138, v138, s76, v213
	v_med3_f32 v143, v143, s76, v213
	v_med3_f32 v139, v139, s76, v213
	v_pk_mul_f32 v[24:25], v[24:25], v[142:143]
	v_pk_mul_f32 v[26:27], v[26:27], v[138:139]
	v_pk_add_f32 v[138:139], v[158:159], 1.0 op_sel_hi:[1,0]
	v_pk_add_f32 v[142:143], v[160:161], 1.0 op_sel_hi:[1,0]
	v_rcp_f32_e32 v138, v138
	v_rcp_f32_e32 v142, v142
	v_rcp_f32_e32 v139, v139
	v_rcp_f32_e32 v143, v143
	v_pk_mul_f32 v[24:25], v[24:25], v[140:141]
	v_pk_mul_f32 v[26:27], v[26:27], v[144:145]
	v_cvt_pk_fp8_f32 v32, v24, v25
	v_cvt_pk_fp8_f32 v33, v26, v27
	v_pk_mul_f32 v[24:25], v[28:29], v[138:139]
	v_pk_mul_f32 v[26:27], v[30:31], v[142:143]
	v_cvt_pk_fp8_f32 v32, v24, v25 op_sel:[0,0,1]
	v_cvt_pk_fp8_f32 v33, v26, v27 op_sel:[0,0,1]
	v_pk_fma_f32 v[152:153], v[152:153], s[22:23], v[8:9] op_sel_hi:[1,0,1]
	v_pk_fma_f32 v[150:151], v[150:151], s[22:23], v[10:11] op_sel_hi:[1,0,1]
	v_pk_fma_f32 v[148:149], v[148:149], s[22:23], v[4:5] op_sel_hi:[1,0,1]
	v_pk_fma_f32 v[146:147], v[146:147], s[22:23], v[6:7] op_sel_hi:[1,0,1]
	v_min_f32_e32 v150, 0x42600000, v150
	v_pk_fma_f32 v[134:135], v[134:135], s[24:25], v[18:19] op_sel_hi:[1,0,1]
	v_min_f32_e32 v28, 0x42600000, v152
	v_min_f32_e32 v146, 0x42600000, v146
	v_pk_fma_f32 v[136:137], v[136:137], s[24:25], v[16:17] op_sel_hi:[1,0,1]
	v_pk_fma_f32 v[132:133], v[132:133], s[24:25], v[12:13] op_sel_hi:[1,0,1]
	v_med3_f32 v27, v135, s76, v213
	v_min_f32_e32 v30, 0x42600000, v148
	v_mul_f32_e32 v23, 0xbe9d265f, v150
	v_mul_f32_e32 v135, 0xbe9d265f, v28
	v_pk_fma_f32 v[24:25], v[130:131], s[24:25], v[14:15] op_sel_hi:[1,0,1]
	global_store_dwordx2 v[2:3], v[32:33], off
	v_min_f32_e32 v151, 0x42600000, v151
	v_med3_f32 v32, v136, s76, v213
	v_med3_f32 v130, v132, s76, v213
	v_min_f32_e32 v29, 0x42600000, v153
	v_exp_f32_e32 v132, v23
	v_mul_f32_e32 v23, 0xbe9d265f, v146
	v_exp_f32_e32 v136, v135
	v_mul_f32_e32 v135, 0xbe9d265f, v30
	v_med3_f32 v26, v134, s76, v213
	v_min_f32_e32 v147, 0x42600000, v147
	v_min_f32_e32 v31, 0x42600000, v149
	v_exp_f32_e32 v134, v23
	v_mul_f32_e32 v23, 0xbe9d265f, v151
	v_exp_f32_e32 v138, v135
	v_mul_f32_e32 v135, 0xbe9d265f, v29
	v_med3_f32 v33, v137, s76, v213
	v_med3_f32 v131, v133, s76, v213
	v_exp_f32_e32 v133, v23
	v_mul_f32_e32 v23, 0xbe9d265f, v147
	v_exp_f32_e32 v137, v135
	v_mul_f32_e32 v135, 0xbe9d265f, v31
	v_exp_f32_e32 v139, v135
	v_exp_f32_e32 v135, v23
	v_pk_add_f32 v[132:133], v[132:133], 1.0 op_sel_hi:[1,0]
	v_med3_f32 v24, v24, s76, v213
	v_rcp_f32_e32 v132, v132
	v_pk_add_f32 v[134:135], v[134:135], 1.0 op_sel_hi:[1,0]
	v_rcp_f32_e32 v133, v133
	v_rcp_f32_e32 v134, v134
	v_rcp_f32_e32 v135, v135
	v_med3_f32 v25, v25, s76, v213
	v_pk_add_f32 v[138:139], v[138:139], 1.0 op_sel_hi:[1,0]
	v_pk_mul_f32 v[24:25], v[146:147], v[24:25]
	v_pk_add_f32 v[136:137], v[136:137], 1.0 op_sel_hi:[1,0]
	v_rcp_f32_e32 v138, v138
	v_rcp_f32_e32 v139, v139
	v_pk_mul_f32 v[28:29], v[28:29], v[32:33]
	v_pk_mul_f32 v[26:27], v[150:151], v[26:27]
	v_pk_mul_f32 v[24:25], v[24:25], v[134:135]
	v_mov_b32_e32 v33, v163
	v_rcp_f32_e32 v136, v136
	v_rcp_f32_e32 v137, v137
	v_pk_mul_f32 v[26:27], v[26:27], v[132:133]
	v_mov_b32_e32 v32, v163
	v_cvt_pk_fp8_f32 v33, v24, v25
	v_cvt_pk_fp8_f32 v32, v26, v27
	v_pk_mul_f32 v[24:25], v[30:31], v[130:131]
	v_pk_mul_f32 v[28:29], v[28:29], v[136:137]
	v_pk_mul_f32 v[24:25], v[24:25], v[138:139]
	v_cvt_pk_fp8_f32 v32, v28, v29 op_sel:[0,0,1]
	v_cvt_pk_fp8_f32 v33, v24, v25 op_sel:[0,0,1]
	v_or_b32_e32 v24, 16, v22
	v_ashrrev_i32_e32 v25, 31, v24
	v_lshlrev_b64 v[24:25], 11, v[24:25]
	v_lshl_add_u64 v[24:25], s[14:15], 0, v[24:25]
	v_lshl_add_u64 v[24:25], v[24:25], 0, v[20:21]
	global_store_dwordx2 v[24:25], v[32:33], off
	v_pk_fma_f32 v[24:25], v[128:129], s[22:23], v[8:9] op_sel_hi:[1,0,1]
	v_pk_fma_f32 v[26:27], v[126:127], s[22:23], v[10:11] op_sel_hi:[1,0,1]
	v_pk_fma_f32 v[28:29], v[124:125], s[22:23], v[4:5] op_sel_hi:[1,0,1]
	v_pk_fma_f32 v[30:31], v[122:123], s[22:23], v[6:7] op_sel_hi:[1,0,1]
	v_min_f32_e32 v26, 0x42600000, v26
	v_min_f32_e32 v24, 0x42600000, v24
	v_min_f32_e32 v30, 0x42600000, v30
	v_min_f32_e32 v28, 0x42600000, v28
	v_mul_f32_e32 v23, 0xbe9d265f, v26
	v_mul_f32_e32 v123, 0xbe9d265f, v24
	v_pk_fma_f32 v[32:33], v[120:121], s[24:25], v[16:17] op_sel_hi:[1,0,1]
	v_min_f32_e32 v27, 0x42600000, v27
	v_min_f32_e32 v25, 0x42600000, v25
	v_exp_f32_e32 v120, v23
	v_mul_f32_e32 v23, 0xbe9d265f, v30
	v_exp_f32_e32 v124, v123
	v_mul_f32_e32 v123, 0xbe9d265f, v28
	v_min_f32_e32 v31, 0x42600000, v31
	v_min_f32_e32 v29, 0x42600000, v29
	v_exp_f32_e32 v122, v23
	v_mul_f32_e32 v23, 0xbe9d265f, v27
	v_exp_f32_e32 v126, v123
	v_mul_f32_e32 v123, 0xbe9d265f, v25
	v_exp_f32_e32 v121, v23
	v_mul_f32_e32 v23, 0xbe9d265f, v31
	v_exp_f32_e32 v125, v123
	v_mul_f32_e32 v123, 0xbe9d265f, v29
	v_exp_f32_e32 v127, v123
	v_exp_f32_e32 v123, v23
	v_pk_add_f32 v[120:121], v[120:121], 1.0 op_sel_hi:[1,0]
	v_pk_fma_f32 v[118:119], v[118:119], s[24:25], v[18:19] op_sel_hi:[1,0,1]
	v_rcp_f32_e32 v120, v120
	v_pk_add_f32 v[122:123], v[122:123], 1.0 op_sel_hi:[1,0]
	v_rcp_f32_e32 v121, v121
	v_rcp_f32_e32 v122, v122
	v_rcp_f32_e32 v123, v123
	v_pk_fma_f32 v[114:115], v[114:115], s[24:25], v[14:15] op_sel_hi:[1,0,1]
	v_med3_f32 v118, v118, s76, v213
	v_med3_f32 v119, v119, s76, v213
	v_med3_f32 v114, v114, s76, v213
	v_med3_f32 v115, v115, s76, v213
	v_med3_f32 v32, v32, s76, v213
	v_med3_f32 v33, v33, s76, v213
	v_pk_add_f32 v[124:125], v[124:125], 1.0 op_sel_hi:[1,0]
	v_pk_mul_f32 v[26:27], v[26:27], v[118:119]
	v_pk_add_f32 v[126:127], v[126:127], 1.0 op_sel_hi:[1,0]
	v_rcp_f32_e32 v124, v124
	v_rcp_f32_e32 v125, v125
	v_pk_mul_f32 v[24:25], v[24:25], v[32:33]
	v_pk_mul_f32 v[26:27], v[26:27], v[120:121]
	v_pk_mul_f32 v[30:31], v[30:31], v[114:115]
	v_mov_b32_e32 v32, v163
	v_rcp_f32_e32 v126, v126
	v_rcp_f32_e32 v127, v127
	v_pk_mul_f32 v[30:31], v[30:31], v[122:123]
	v_cvt_pk_fp8_f32 v32, v26, v27
	v_mov_b32_e32 v33, v163
	v_pk_fma_f32 v[116:117], v[116:117], s[24:25], v[12:13] op_sel_hi:[1,0,1]
	v_cvt_pk_fp8_f32 v33, v30, v31
	v_med3_f32 v116, v116, s76, v213
	v_med3_f32 v117, v117, s76, v213
	v_pk_mul_f32 v[24:25], v[24:25], v[124:125]
	v_pk_mul_f32 v[26:27], v[28:29], v[116:117]
	v_cvt_pk_fp8_f32 v32, v24, v25 op_sel:[0,0,1]
	v_pk_mul_f32 v[26:27], v[26:27], v[126:127]
	v_or_b32_e32 v24, 32, v22
	v_cvt_pk_fp8_f32 v33, v26, v27 op_sel:[0,0,1]
	v_ashrrev_i32_e32 v25, 31, v24
	v_lshlrev_b64 v[24:25], 11, v[24:25]
	v_lshl_add_u64 v[24:25], s[14:15], 0, v[24:25]
	v_lshl_add_u64 v[24:25], v[24:25], 0, v[20:21]
	global_store_dwordx2 v[24:25], v[32:33], off
	v_pk_fma_f32 v[24:25], v[112:113], s[22:23], v[8:9] op_sel_hi:[1,0,1]
	v_pk_fma_f32 v[26:27], v[110:111], s[22:23], v[10:11] op_sel_hi:[1,0,1]
	v_pk_fma_f32 v[28:29], v[108:109], s[22:23], v[4:5] op_sel_hi:[1,0,1]
	v_pk_fma_f32 v[30:31], v[106:107], s[22:23], v[6:7] op_sel_hi:[1,0,1]
	v_min_f32_e32 v26, 0x42600000, v26
	v_min_f32_e32 v24, 0x42600000, v24
	v_min_f32_e32 v30, 0x42600000, v30
	v_min_f32_e32 v28, 0x42600000, v28
	v_mul_f32_e32 v23, 0xbe9d265f, v26
	v_mul_f32_e32 v107, 0xbe9d265f, v24
	v_pk_fma_f32 v[32:33], v[104:105], s[24:25], v[16:17] op_sel_hi:[1,0,1]
	v_min_f32_e32 v27, 0x42600000, v27
	v_min_f32_e32 v25, 0x42600000, v25
	v_exp_f32_e32 v104, v23
	v_mul_f32_e32 v23, 0xbe9d265f, v30
	v_exp_f32_e32 v108, v107
	v_mul_f32_e32 v107, 0xbe9d265f, v28
	v_min_f32_e32 v31, 0x42600000, v31
	v_min_f32_e32 v29, 0x42600000, v29
	v_exp_f32_e32 v106, v23
	v_mul_f32_e32 v23, 0xbe9d265f, v27
	v_exp_f32_e32 v110, v107
	v_mul_f32_e32 v107, 0xbe9d265f, v25
	v_exp_f32_e32 v105, v23
	v_mul_f32_e32 v23, 0xbe9d265f, v31
	v_exp_f32_e32 v109, v107
	v_mul_f32_e32 v107, 0xbe9d265f, v29
	v_exp_f32_e32 v111, v107
	v_exp_f32_e32 v107, v23
	v_pk_add_f32 v[104:105], v[104:105], 1.0 op_sel_hi:[1,0]
	v_pk_fma_f32 v[102:103], v[102:103], s[24:25], v[18:19] op_sel_hi:[1,0,1]
	v_rcp_f32_e32 v104, v104
	v_pk_add_f32 v[106:107], v[106:107], 1.0 op_sel_hi:[1,0]
	v_rcp_f32_e32 v105, v105
	v_rcp_f32_e32 v106, v106
	v_rcp_f32_e32 v107, v107
	v_pk_fma_f32 v[98:99], v[98:99], s[24:25], v[14:15] op_sel_hi:[1,0,1]
	v_med3_f32 v102, v102, s76, v213
	v_med3_f32 v98, v98, s76, v213
	v_med3_f32 v103, v103, s76, v213
	v_med3_f32 v99, v99, s76, v213
	v_med3_f32 v32, v32, s76, v213
	v_med3_f32 v33, v33, s76, v213
	v_pk_add_f32 v[108:109], v[108:109], 1.0 op_sel_hi:[1,0]
	v_pk_add_f32 v[110:111], v[110:111], 1.0 op_sel_hi:[1,0]
	v_pk_mul_f32 v[26:27], v[26:27], v[102:103]
	v_pk_mul_f32 v[30:31], v[30:31], v[98:99]
	v_rcp_f32_e32 v108, v108
	v_rcp_f32_e32 v110, v110
	v_rcp_f32_e32 v109, v109
	v_rcp_f32_e32 v111, v111
	v_pk_mul_f32 v[24:25], v[24:25], v[32:33]
	v_pk_mul_f32 v[26:27], v[26:27], v[104:105]
	v_pk_mul_f32 v[30:31], v[30:31], v[106:107]
	v_mov_b32_e32 v32, v163
	v_mov_b32_e32 v33, v163
	v_pk_fma_f32 v[100:101], v[100:101], s[24:25], v[12:13] op_sel_hi:[1,0,1]
	v_cvt_pk_fp8_f32 v32, v26, v27
	v_cvt_pk_fp8_f32 v33, v30, v31
	v_med3_f32 v100, v100, s76, v213
	v_med3_f32 v101, v101, s76, v213
	v_pk_mul_f32 v[26:27], v[28:29], v[100:101]
	v_pk_mul_f32 v[24:25], v[24:25], v[108:109]
	v_pk_mul_f32 v[26:27], v[26:27], v[110:111]
	v_or_b32_e32 v22, 48, v22
	v_cvt_pk_fp8_f32 v32, v24, v25 op_sel:[0,0,1]
	v_cvt_pk_fp8_f32 v33, v26, v27 op_sel:[0,0,1]
	v_ashrrev_i32_e32 v23, 31, v22
	v_lshlrev_b64 v[22:23], 11, v[22:23]
	v_lshl_add_u64 v[22:23], s[14:15], 0, v[22:23]
	v_pk_fma_f32 v[26:27], v[90:91], s[22:23], v[6:7] op_sel_hi:[1,0,1]
	v_lshl_add_u64 v[20:21], v[22:23], 0, v[20:21]
	v_pk_fma_f32 v[22:23], v[94:95], s[22:23], v[10:11] op_sel_hi:[1,0,1]
	v_min_f32_e32 v26, 0x42600000, v26
	global_store_dwordx2 v[20:21], v[32:33], off
	v_pk_fma_f32 v[32:33], v[84:85], s[24:25], v[12:13] op_sel_hi:[1,0,1]
	v_min_f32_e32 v22, 0x42600000, v22
	v_min_f32_e32 v23, 0x42600000, v23
	v_min_f32_e32 v27, 0x42600000, v27
	v_mul_f32_e32 v85, 0xbe9d265f, v26
	v_pk_fma_f32 v[30:31], v[86:87], s[24:25], v[18:19] op_sel_hi:[1,0,1]
	v_mul_f32_e32 v84, 0xbe9d265f, v22
	v_exp_f32_e32 v86, v85
	v_mul_f32_e32 v85, 0xbe9d265f, v23
	v_mul_f32_e32 v87, 0xbe9d265f, v27
	v_pk_fma_f32 v[24:25], v[92:93], s[22:23], v[4:5] op_sel_hi:[1,0,1]
	v_exp_f32_e32 v84, v84
	v_exp_f32_e32 v85, v85
	v_exp_f32_e32 v87, v87
	v_pk_fma_f32 v[20:21], v[96:97], s[22:23], v[8:9] op_sel_hi:[1,0,1]
	v_min_f32_e32 v24, 0x42600000, v24
	v_pk_fma_f32 v[28:29], v[88:89], s[24:25], v[16:17] op_sel_hi:[1,0,1]
	v_min_f32_e32 v20, 0x42600000, v20
	v_min_f32_e32 v21, 0x42600000, v21
	v_min_f32_e32 v25, 0x42600000, v25
	v_mul_f32_e32 v89, 0xbe9d265f, v24
	v_mul_f32_e32 v88, 0xbe9d265f, v20
	v_exp_f32_e32 v90, v89
	v_mul_f32_e32 v89, 0xbe9d265f, v21
	v_mul_f32_e32 v91, 0xbe9d265f, v25
	v_exp_f32_e32 v88, v88
	v_exp_f32_e32 v89, v89
	v_exp_f32_e32 v91, v91
	v_pk_add_f32 v[84:85], v[84:85], 1.0 op_sel_hi:[1,0]
	v_pk_add_f32 v[86:87], v[86:87], 1.0 op_sel_hi:[1,0]
	v_rcp_f32_e32 v84, v84
	v_rcp_f32_e32 v86, v86
	v_rcp_f32_e32 v85, v85
	v_rcp_f32_e32 v87, v87
	v_pk_fma_f32 v[82:83], v[82:83], s[24:25], v[14:15] op_sel_hi:[1,0,1]
	v_med3_f32 v30, v30, s76, v213
	v_med3_f32 v82, v82, s76, v213
	v_med3_f32 v31, v31, s76, v213
	v_med3_f32 v83, v83, s76, v213
	v_med3_f32 v28, v28, s76, v213
	v_med3_f32 v29, v29, s76, v213
	v_pk_add_f32 v[88:89], v[88:89], 1.0 op_sel_hi:[1,0]
	v_pk_add_f32 v[90:91], v[90:91], 1.0 op_sel_hi:[1,0]
	v_pk_mul_f32 v[22:23], v[22:23], v[30:31]
	v_pk_mul_f32 v[26:27], v[26:27], v[82:83]
	v_rcp_f32_e32 v88, v88
	v_rcp_f32_e32 v90, v90
	v_rcp_f32_e32 v89, v89
	v_rcp_f32_e32 v91, v91
	v_pk_mul_f32 v[20:21], v[20:21], v[28:29]
	v_pk_mul_f32 v[22:23], v[22:23], v[84:85]
	v_pk_mul_f32 v[26:27], v[26:27], v[86:87]
	v_mov_b32_e32 v28, v163
	v_mov_b32_e32 v29, v163
	v_cvt_pk_fp8_f32 v28, v22, v23
	v_cvt_pk_fp8_f32 v29, v26, v27
	v_med3_f32 v32, v32, s76, v213
	v_med3_f32 v33, v33, s76, v213
	v_pk_mul_f32 v[22:23], v[24:25], v[32:33]
	v_pk_mul_f32 v[20:21], v[20:21], v[88:89]
	v_pk_mul_f32 v[22:23], v[22:23], v[90:91]
	v_pk_fma_f32 v[26:27], v[74:75], s[22:23], v[6:7] op_sel_hi:[1,0,1]
	v_cvt_pk_fp8_f32 v28, v20, v21 op_sel:[0,0,1]
	v_cvt_pk_fp8_f32 v29, v22, v23 op_sel:[0,0,1]
	v_pk_fma_f32 v[22:23], v[78:79], s[22:23], v[10:11] op_sel_hi:[1,0,1]
	v_min_f32_e32 v26, 0x42600000, v26
	v_pk_fma_f32 v[32:33], v[68:69], s[24:25], v[12:13] op_sel_hi:[1,0,1]
	v_min_f32_e32 v22, 0x42600000, v22
	v_min_f32_e32 v23, 0x42600000, v23
	v_min_f32_e32 v27, 0x42600000, v27
	v_mul_f32_e32 v69, 0xbe9d265f, v26
	v_add_co_u32_e32 v20, vcc, s77, v2
	v_pk_fma_f32 v[30:31], v[70:71], s[24:25], v[18:19] op_sel_hi:[1,0,1]
	v_mul_f32_e32 v68, 0xbe9d265f, v22
	v_exp_f32_e32 v70, v69
	v_mul_f32_e32 v69, 0xbe9d265f, v23
	v_mul_f32_e32 v71, 0xbe9d265f, v27
	v_addc_co_u32_e32 v21, vcc, 0, v3, vcc
	v_pk_fma_f32 v[24:25], v[76:77], s[22:23], v[4:5] op_sel_hi:[1,0,1]
	v_exp_f32_e32 v68, v68
	v_exp_f32_e32 v69, v69
	v_exp_f32_e32 v71, v71
	global_store_dwordx2 v[20:21], v[28:29], off
	v_pk_fma_f32 v[20:21], v[80:81], s[22:23], v[8:9] op_sel_hi:[1,0,1]
	v_min_f32_e32 v24, 0x42600000, v24
	v_pk_fma_f32 v[28:29], v[72:73], s[24:25], v[16:17] op_sel_hi:[1,0,1]
	v_min_f32_e32 v20, 0x42600000, v20
	v_min_f32_e32 v21, 0x42600000, v21
	v_min_f32_e32 v25, 0x42600000, v25
	v_mul_f32_e32 v73, 0xbe9d265f, v24
	v_mul_f32_e32 v72, 0xbe9d265f, v20
	v_exp_f32_e32 v74, v73
	v_mul_f32_e32 v73, 0xbe9d265f, v21
	v_mul_f32_e32 v75, 0xbe9d265f, v25
	v_exp_f32_e32 v72, v72
	v_exp_f32_e32 v73, v73
	v_exp_f32_e32 v75, v75
	v_pk_add_f32 v[68:69], v[68:69], 1.0 op_sel_hi:[1,0]
	v_pk_add_f32 v[70:71], v[70:71], 1.0 op_sel_hi:[1,0]
	v_rcp_f32_e32 v68, v68
	v_rcp_f32_e32 v70, v70
	v_rcp_f32_e32 v69, v69
	v_rcp_f32_e32 v71, v71
	v_pk_fma_f32 v[66:67], v[66:67], s[24:25], v[14:15] op_sel_hi:[1,0,1]
	v_med3_f32 v30, v30, s76, v213
	v_med3_f32 v66, v66, s76, v213
	v_med3_f32 v31, v31, s76, v213
	v_med3_f32 v67, v67, s76, v213
	v_med3_f32 v28, v28, s76, v213
	v_med3_f32 v29, v29, s76, v213
	v_pk_add_f32 v[72:73], v[72:73], 1.0 op_sel_hi:[1,0]
	v_pk_add_f32 v[74:75], v[74:75], 1.0 op_sel_hi:[1,0]
	v_pk_mul_f32 v[22:23], v[22:23], v[30:31]
	v_pk_mul_f32 v[26:27], v[26:27], v[66:67]
	v_rcp_f32_e32 v72, v72
	v_rcp_f32_e32 v74, v74
	v_rcp_f32_e32 v73, v73
	v_rcp_f32_e32 v75, v75
	v_pk_mul_f32 v[20:21], v[20:21], v[28:29]
	v_pk_mul_f32 v[22:23], v[22:23], v[68:69]
	v_pk_mul_f32 v[26:27], v[26:27], v[70:71]
	v_mov_b32_e32 v28, v163
	v_mov_b32_e32 v29, v163
	v_cvt_pk_fp8_f32 v28, v22, v23
	v_cvt_pk_fp8_f32 v29, v26, v27
	v_med3_f32 v32, v32, s76, v213
	v_med3_f32 v33, v33, s76, v213
	v_pk_mul_f32 v[22:23], v[24:25], v[32:33]
	v_pk_mul_f32 v[20:21], v[20:21], v[72:73]
	v_pk_mul_f32 v[22:23], v[22:23], v[74:75]
	v_pk_fma_f32 v[26:27], v[58:59], s[22:23], v[6:7] op_sel_hi:[1,0,1]
	v_cvt_pk_fp8_f32 v28, v20, v21 op_sel:[0,0,1]
	v_cvt_pk_fp8_f32 v29, v22, v23 op_sel:[0,0,1]
	v_pk_fma_f32 v[22:23], v[62:63], s[22:23], v[10:11] op_sel_hi:[1,0,1]
	v_min_f32_e32 v26, 0x42600000, v26
	v_pk_fma_f32 v[32:33], v[52:53], s[24:25], v[12:13] op_sel_hi:[1,0,1]
	v_min_f32_e32 v22, 0x42600000, v22
	v_min_f32_e32 v23, 0x42600000, v23
	v_min_f32_e32 v27, 0x42600000, v27
	v_mul_f32_e32 v53, 0xbe9d265f, v26
	v_add_co_u32_e32 v20, vcc, s78, v2
	v_pk_fma_f32 v[30:31], v[54:55], s[24:25], v[18:19] op_sel_hi:[1,0,1]
	v_mul_f32_e32 v52, 0xbe9d265f, v22
	v_exp_f32_e32 v54, v53
	v_mul_f32_e32 v53, 0xbe9d265f, v23
	v_mul_f32_e32 v55, 0xbe9d265f, v27
	v_addc_co_u32_e32 v21, vcc, 0, v3, vcc
	v_pk_fma_f32 v[24:25], v[60:61], s[22:23], v[4:5] op_sel_hi:[1,0,1]
	v_exp_f32_e32 v52, v52
	v_exp_f32_e32 v53, v53
	v_exp_f32_e32 v55, v55
	global_store_dwordx2 v[20:21], v[28:29], off
	v_pk_fma_f32 v[20:21], v[64:65], s[22:23], v[8:9] op_sel_hi:[1,0,1]
	v_min_f32_e32 v24, 0x42600000, v24
	v_pk_fma_f32 v[28:29], v[56:57], s[24:25], v[16:17] op_sel_hi:[1,0,1]
	v_min_f32_e32 v20, 0x42600000, v20
	v_min_f32_e32 v21, 0x42600000, v21
	v_min_f32_e32 v25, 0x42600000, v25
	v_mul_f32_e32 v57, 0xbe9d265f, v24
	v_mul_f32_e32 v56, 0xbe9d265f, v20
	v_exp_f32_e32 v58, v57
	v_mul_f32_e32 v57, 0xbe9d265f, v21
	v_mul_f32_e32 v59, 0xbe9d265f, v25
	v_exp_f32_e32 v56, v56
	v_exp_f32_e32 v57, v57
	v_exp_f32_e32 v59, v59
	v_pk_add_f32 v[52:53], v[52:53], 1.0 op_sel_hi:[1,0]
	v_pk_add_f32 v[54:55], v[54:55], 1.0 op_sel_hi:[1,0]
	v_rcp_f32_e32 v52, v52
	v_rcp_f32_e32 v54, v54
	v_rcp_f32_e32 v53, v53
	v_rcp_f32_e32 v55, v55
	v_pk_fma_f32 v[50:51], v[50:51], s[24:25], v[14:15] op_sel_hi:[1,0,1]
	v_med3_f32 v30, v30, s76, v213
	v_med3_f32 v50, v50, s76, v213
	v_med3_f32 v31, v31, s76, v213
	v_med3_f32 v51, v51, s76, v213
	v_med3_f32 v28, v28, s76, v213
	v_med3_f32 v29, v29, s76, v213
	v_pk_add_f32 v[56:57], v[56:57], 1.0 op_sel_hi:[1,0]
	v_pk_add_f32 v[58:59], v[58:59], 1.0 op_sel_hi:[1,0]
	v_pk_mul_f32 v[22:23], v[22:23], v[30:31]
	v_pk_mul_f32 v[26:27], v[26:27], v[50:51]
	v_rcp_f32_e32 v56, v56
	v_rcp_f32_e32 v58, v58
	v_rcp_f32_e32 v57, v57
	v_rcp_f32_e32 v59, v59
	v_pk_mul_f32 v[20:21], v[20:21], v[28:29]
	v_pk_mul_f32 v[22:23], v[22:23], v[52:53]
	v_pk_mul_f32 v[26:27], v[26:27], v[54:55]
	v_mov_b32_e32 v28, v163
	v_mov_b32_e32 v29, v163
	v_cvt_pk_fp8_f32 v28, v22, v23
	v_cvt_pk_fp8_f32 v29, v26, v27
	v_med3_f32 v32, v32, s76, v213
	v_med3_f32 v33, v33, s76, v213
	v_pk_mul_f32 v[22:23], v[24:25], v[32:33]
	v_pk_mul_f32 v[20:21], v[20:21], v[56:57]
	v_pk_mul_f32 v[22:23], v[22:23], v[58:59]
	v_cvt_pk_fp8_f32 v28, v20, v21 op_sel:[0,0,1]
	v_cvt_pk_fp8_f32 v29, v22, v23 op_sel:[0,0,1]
	v_add_co_u32_e32 v20, vcc, s79, v2
	v_pk_fma_f32 v[6:7], v[42:43], s[22:23], v[6:7] op_sel_hi:[1,0,1]
	s_nop 0
	v_addc_co_u32_e32 v21, vcc, 0, v3, vcc
	v_pk_fma_f32 v[10:11], v[46:47], s[22:23], v[10:11] op_sel_hi:[1,0,1]
	v_min_f32_e32 v6, 0x42600000, v6
	global_store_dwordx2 v[20:21], v[28:29], off
	v_min_f32_e32 v10, 0x42600000, v10
	v_min_f32_e32 v11, 0x42600000, v11
	v_min_f32_e32 v7, 0x42600000, v7
	v_mul_f32_e32 v21, 0xbe9d265f, v6
	v_mul_f32_e32 v20, 0xbe9d265f, v10
	v_exp_f32_e32 v22, v21
	v_mul_f32_e32 v21, 0xbe9d265f, v11
	v_mul_f32_e32 v23, 0xbe9d265f, v7
	v_pk_fma_f32 v[4:5], v[44:45], s[22:23], v[4:5] op_sel_hi:[1,0,1]
	v_exp_f32_e32 v20, v20
	v_exp_f32_e32 v21, v21
	v_exp_f32_e32 v23, v23
	v_pk_fma_f32 v[8:9], v[48:49], s[22:23], v[8:9] op_sel_hi:[1,0,1]
	v_min_f32_e32 v4, 0x42600000, v4
	v_min_f32_e32 v8, 0x42600000, v8
	v_min_f32_e32 v9, 0x42600000, v9
	v_min_f32_e32 v5, 0x42600000, v5
	v_mul_f32_e32 v25, 0xbe9d265f, v4
	v_mul_f32_e32 v24, 0xbe9d265f, v8
	v_exp_f32_e32 v26, v25
	v_mul_f32_e32 v25, 0xbe9d265f, v9
	v_mul_f32_e32 v27, 0xbe9d265f, v5
	v_exp_f32_e32 v24, v24
	v_exp_f32_e32 v25, v25
	v_exp_f32_e32 v27, v27
	v_pk_add_f32 v[20:21], v[20:21], 1.0 op_sel_hi:[1,0]
	v_pk_add_f32 v[22:23], v[22:23], 1.0 op_sel_hi:[1,0]
	v_rcp_f32_e32 v20, v20
	v_rcp_f32_e32 v22, v22
	v_rcp_f32_e32 v21, v21
	v_rcp_f32_e32 v23, v23
	v_pk_fma_f32 v[18:19], v[38:39], s[24:25], v[18:19] op_sel_hi:[1,0,1]
	v_pk_fma_f32 v[14:15], v[34:35], s[24:25], v[14:15] op_sel_hi:[1,0,1]
	v_med3_f32 v18, v18, s76, v213
	v_med3_f32 v14, v14, s76, v213
	v_med3_f32 v19, v19, s76, v213
	v_med3_f32 v15, v15, s76, v213
	v_pk_add_f32 v[24:25], v[24:25], 1.0 op_sel_hi:[1,0]
	v_pk_add_f32 v[26:27], v[26:27], 1.0 op_sel_hi:[1,0]
	v_pk_mul_f32 v[10:11], v[10:11], v[18:19]
	v_pk_mul_f32 v[6:7], v[6:7], v[14:15]
	v_rcp_f32_e32 v24, v24
	v_rcp_f32_e32 v26, v26
	v_rcp_f32_e32 v25, v25
	v_rcp_f32_e32 v27, v27
	v_pk_mul_f32 v[10:11], v[10:11], v[20:21]
	v_pk_mul_f32 v[6:7], v[6:7], v[22:23]
	v_mov_b32_e32 v14, v163
	v_mov_b32_e32 v15, v163
	v_pk_fma_f32 v[16:17], v[40:41], s[24:25], v[16:17] op_sel_hi:[1,0,1]
	v_pk_fma_f32 v[12:13], v[36:37], s[24:25], v[12:13] op_sel_hi:[1,0,1]
	v_cvt_pk_fp8_f32 v14, v10, v11
	v_cvt_pk_fp8_f32 v15, v6, v7
	v_med3_f32 v16, v16, s76, v213
	v_med3_f32 v12, v12, s76, v213
	v_med3_f32 v17, v17, s76, v213
	v_med3_f32 v13, v13, s76, v213
	v_pk_mul_f32 v[8:9], v[8:9], v[16:17]
	v_pk_mul_f32 v[4:5], v[4:5], v[12:13]
	v_pk_mul_f32 v[8:9], v[8:9], v[24:25]
	v_pk_mul_f32 v[4:5], v[4:5], v[26:27]
	v_cvt_pk_fp8_f32 v14, v8, v9 op_sel:[0,0,1]
	v_cvt_pk_fp8_f32 v15, v4, v5 op_sel:[0,0,1]
	v_add_co_u32_e32 v2, vcc, 0x58000, v2
	s_nop 1
	v_addc_co_u32_e32 v3, vcc, 0, v3, vcc
	s_andn2_b64 vcc, exec, s[98:99]
	global_store_dwordx2 v[2:3], v[14:15], off
	s_cbranch_vccnz .LBB0_786
	s_branch .Lp6_entry_pre

.LBB0_868:
	s_waitcnt vmcnt(0)
	v_pk_mul_f32 v[30:31], v[10:11], s[22:23] op_sel_hi:[1,0]
	s_nop 0
	v_pk_fma_f32 v[32:33], v[158:159], s[24:25], v[30:31] op_sel_hi:[1,0,1]
	v_pk_mul_f32 v[12:13], v[12:13], s[22:23] op_sel_hi:[1,0]
	v_med3_f32 v21, v32, s74, v215
	v_med3_f32 v29, v33, s74, v215
	v_cvt_pk_fp8_f32 v22, v21, v29
	v_pk_mul_f32 v[14:15], v[14:15], s[22:23] op_sel_hi:[1,0]
	v_pk_fma_f32 v[10:11], v[160:161], s[24:25], v[12:13] op_sel_hi:[1,0,1]
	v_pk_fma_f32 v[130:131], v[130:131], s[24:25], v[14:15] op_sel_hi:[1,0,1]
	v_med3_f32 v10, v10, s74, v215
	v_med3_f32 v11, v11, s74, v215
	v_pk_fma_f32 v[154:155], v[154:155], s[24:25], v[14:15] op_sel_hi:[1,0,1]
	v_med3_f32 v130, v130, s74, v215
	v_cvt_pk_fp8_f32 v22, v10, v11 op_sel:[0,0,1]
	v_med3_f32 v10, v131, s74, v215
	v_mov_b32_e32 v29, 0
	v_pk_fma_f32 v[150:151], v[150:151], s[24:25], v[30:31] op_sel_hi:[1,0,1]
	v_pk_fma_f32 v[146:147], v[146:147], s[24:25], v[14:15] op_sel_hi:[1,0,1]
	v_med3_f32 v32, v154, s74, v215
	v_med3_f32 v33, v155, s74, v215
	v_cvt_pk_fp8_f32 v29, v130, v10
	v_pk_mul_f32 v[16:17], v[16:17], s[22:23] op_sel_hi:[1,0]
	v_pk_fma_f32 v[142:143], v[142:143], s[24:25], v[30:31] op_sel_hi:[1,0,1]
	v_pk_fma_f32 v[138:139], v[138:139], s[24:25], v[14:15] op_sel_hi:[1,0,1]
	v_med3_f32 v150, v150, s74, v215
	v_med3_f32 v151, v151, s74, v215
	v_med3_f32 v146, v146, s74, v215
	v_med3_f32 v147, v147, s74, v215
	v_cvt_pk_fp8_f32 v23, v32, v33
	v_pk_fma_f32 v[132:133], v[132:133], s[24:25], v[16:17] op_sel_hi:[1,0,1]
	v_med3_f32 v142, v142, s74, v215
	v_med3_f32 v143, v143, s74, v215
	v_med3_f32 v138, v138, s74, v215
	v_med3_f32 v139, v139, s74, v215
	v_cvt_pk_fp8_f32 v24, v150, v151
	v_cvt_pk_fp8_f32 v25, v146, v147
	v_pk_fma_f32 v[156:157], v[156:157], s[24:25], v[16:17] op_sel_hi:[1,0,1]
	v_cvt_pk_fp8_f32 v26, v142, v143
	v_cvt_pk_fp8_f32 v27, v138, v139
	v_med3_f32 v10, v132, s74, v215
	v_med3_f32 v11, v133, s74, v215
	v_pk_fma_f32 v[152:153], v[152:153], s[24:25], v[12:13] op_sel_hi:[1,0,1]
	v_pk_fma_f32 v[148:149], v[148:149], s[24:25], v[16:17] op_sel_hi:[1,0,1]
	v_med3_f32 v154, v156, s74, v215
	v_med3_f32 v155, v157, s74, v215
	v_cvt_pk_fp8_f32 v29, v10, v11 op_sel:[0,0,1]
	v_or_b32_e32 v10, 48, v20
	v_pk_fma_f32 v[144:145], v[144:145], s[24:25], v[12:13] op_sel_hi:[1,0,1]
	v_pk_fma_f32 v[140:141], v[140:141], s[24:25], v[16:17] op_sel_hi:[1,0,1]
	v_med3_f32 v152, v152, s74, v215
	v_med3_f32 v153, v153, s74, v215
	v_med3_f32 v148, v148, s74, v215
	v_med3_f32 v149, v149, s74, v215
	v_cvt_pk_fp8_f32 v23, v154, v155 op_sel:[0,0,1]
	v_ashrrev_i32_e32 v11, 31, v10
	v_med3_f32 v144, v144, s74, v215
	v_med3_f32 v145, v145, s74, v215
	v_med3_f32 v140, v140, s74, v215
	v_med3_f32 v141, v141, s74, v215
	v_cvt_pk_fp8_f32 v24, v152, v153 op_sel:[0,0,1]
	v_cvt_pk_fp8_f32 v25, v148, v149 op_sel:[0,0,1]
	v_lshlrev_b64 v[10:11], 11, v[10:11]
	v_cvt_pk_fp8_f32 v26, v144, v145 op_sel:[0,0,1]
	v_cvt_pk_fp8_f32 v27, v140, v141 op_sel:[0,0,1]
	v_lshl_add_u64 v[10:11], s[16:17], 0, v[10:11]
	v_lshl_add_u64 v[10:11], v[10:11], 0, v[18:19]
	v_pk_fma_f32 v[18:19], v[128:129], s[24:25], v[12:13] op_sel_hi:[1,0,1]
	v_pk_fma_f32 v[20:21], v[126:127], s[24:25], v[30:31] op_sel_hi:[1,0,1]
	global_store_dwordx2 v[4:5], v[22:23], off
	global_store_dwordx2 v[6:7], v[24:25], off
	global_store_dwordx2 v[8:9], v[26:27], off
	v_pk_fma_f32 v[24:25], v[122:123], s[24:25], v[14:15] op_sel_hi:[1,0,1]
	v_med3_f32 v20, v20, s74, v215
	v_med3_f32 v21, v21, s74, v215
	v_med3_f32 v26, v18, s74, v215
	v_mov_b32_e32 v18, 0
	v_med3_f32 v27, v19, s74, v215
	v_cvt_pk_fp8_f32 v18, v20, v21
	v_med3_f32 v20, v24, s74, v215
	v_med3_f32 v21, v25, s74, v215
	v_mov_b32_e32 v19, 0
	v_cvt_pk_fp8_f32 v19, v20, v21
	v_pk_fma_f32 v[22:23], v[124:125], s[24:25], v[16:17] op_sel_hi:[1,0,1]
	v_cvt_pk_fp8_f32 v18, v26, v27 op_sel:[0,0,1]
	v_med3_f32 v20, v22, s74, v215
	v_med3_f32 v21, v23, s74, v215
	v_cvt_pk_fp8_f32 v19, v20, v21 op_sel:[0,0,1]
	v_add_co_u32_e32 v20, vcc, s75, v4
	v_pk_fma_f32 v[24:25], v[114:115], s[24:25], v[14:15] op_sel_hi:[1,0,1]
	s_nop 0
	v_addc_co_u32_e32 v21, vcc, 0, v5, vcc
	global_store_dwordx2 v[20:21], v[18:19], off
	v_pk_fma_f32 v[18:19], v[120:121], s[24:25], v[12:13] op_sel_hi:[1,0,1]
	v_pk_fma_f32 v[20:21], v[118:119], s[24:25], v[30:31] op_sel_hi:[1,0,1]
	v_med3_f32 v26, v18, s74, v215
	v_med3_f32 v20, v20, s74, v215
	v_med3_f32 v21, v21, s74, v215
	v_mov_b32_e32 v18, 0
	v_med3_f32 v27, v19, s74, v215
	v_cvt_pk_fp8_f32 v18, v20, v21
	v_med3_f32 v20, v24, s74, v215
	v_med3_f32 v21, v25, s74, v215
	v_mov_b32_e32 v19, 0
	v_cvt_pk_fp8_f32 v19, v20, v21
	v_pk_fma_f32 v[22:23], v[116:117], s[24:25], v[16:17] op_sel_hi:[1,0,1]
	v_cvt_pk_fp8_f32 v18, v26, v27 op_sel:[0,0,1]
	v_med3_f32 v20, v22, s74, v215
	v_med3_f32 v21, v23, s74, v215
	v_cvt_pk_fp8_f32 v19, v20, v21 op_sel:[0,0,1]
	v_add_co_u32_e32 v20, vcc, s76, v4
	v_pk_fma_f32 v[24:25], v[106:107], s[24:25], v[14:15] op_sel_hi:[1,0,1]
	s_nop 0
	v_addc_co_u32_e32 v21, vcc, 0, v5, vcc
	global_store_dwordx2 v[20:21], v[18:19], off
	v_pk_fma_f32 v[18:19], v[112:113], s[24:25], v[12:13] op_sel_hi:[1,0,1]
	v_pk_fma_f32 v[20:21], v[110:111], s[24:25], v[30:31] op_sel_hi:[1,0,1]
	v_med3_f32 v26, v18, s74, v215
	v_med3_f32 v20, v20, s74, v215
	v_med3_f32 v21, v21, s74, v215
	v_mov_b32_e32 v18, 0
	v_med3_f32 v27, v19, s74, v215
	v_cvt_pk_fp8_f32 v18, v20, v21
	v_med3_f32 v20, v24, s74, v215
	v_med3_f32 v21, v25, s74, v215
	v_mov_b32_e32 v19, 0
	v_cvt_pk_fp8_f32 v19, v20, v21
	v_pk_fma_f32 v[22:23], v[108:109], s[24:25], v[16:17] op_sel_hi:[1,0,1]
	v_cvt_pk_fp8_f32 v18, v26, v27 op_sel:[0,0,1]
	v_med3_f32 v20, v22, s74, v215
	v_med3_f32 v21, v23, s74, v215
	v_cvt_pk_fp8_f32 v19, v20, v21 op_sel:[0,0,1]
	v_add_co_u32_e32 v20, vcc, s77, v4
	v_pk_fma_f32 v[136:137], v[136:137], s[24:25], v[12:13] op_sel_hi:[1,0,1]
	s_nop 0
	v_addc_co_u32_e32 v21, vcc, 0, v5, vcc
	v_pk_fma_f32 v[134:135], v[134:135], s[24:25], v[30:31] op_sel_hi:[1,0,1]
	global_store_dwordx2 v[20:21], v[18:19], off
	v_pk_fma_f32 v[12:13], v[100:101], s[24:25], v[12:13] op_sel_hi:[1,0,1]
	v_pk_fma_f32 v[18:19], v[98:99], s[24:25], v[30:31] op_sel_hi:[1,0,1]
	v_pk_fma_f32 v[14:15], v[90:91], s[24:25], v[14:15] op_sel_hi:[1,0,1]
	v_med3_f32 v134, v134, s74, v215
	v_med3_f32 v135, v135, s74, v215
	v_med3_f32 v18, v18, s74, v215
	v_med3_f32 v19, v19, s74, v215
	v_med3_f32 v20, v12, s74, v215
	v_med3_f32 v21, v13, s74, v215
	v_mov_b32_e32 v12, 0
	v_med3_f32 v14, v14, s74, v215
	v_med3_f32 v15, v15, s74, v215
	v_mov_b32_e32 v13, 0
	v_cvt_pk_fp8_f32 v28, v134, v135
	v_cvt_pk_fp8_f32 v12, v18, v19
	v_cvt_pk_fp8_f32 v13, v14, v15
	v_pk_fma_f32 v[16:17], v[92:93], s[24:25], v[16:17] op_sel_hi:[1,0,1]
	v_med3_f32 v136, v136, s74, v215
	v_med3_f32 v137, v137, s74, v215
	v_med3_f32 v14, v16, s74, v215
	v_med3_f32 v15, v17, s74, v215
	v_cvt_pk_fp8_f32 v28, v136, v137 op_sel:[0,0,1]
	v_cvt_pk_fp8_f32 v12, v20, v21 op_sel:[0,0,1]
	v_cvt_pk_fp8_f32 v13, v14, v15 op_sel:[0,0,1]
	v_add_co_u32_e32 v14, vcc, s78, v4
	global_store_dwordx2 v[10:11], v[28:29], off
	s_nop 0
	v_addc_co_u32_e32 v15, vcc, 0, v5, vcc
	global_store_dwordx2 v[14:15], v[12:13], off
	v_lshl_add_u64 v[2:3], v[4:5], 0, s[12:13]
	v_lshl_add_u64 v[20:21], v[4:5], 0, s[26:27]
	v_lshl_add_u64 v[22:23], v[4:5], 0, s[28:29]
	v_lshl_add_u64 v[24:25], v[4:5], 0, s[30:31]
	s_andn2_b64 vcc, exec, s[98:99]
	v_pk_mul_f32 v[14:15], v[194:195], s[22:23] op_sel_hi:[1,0]
	v_pk_mul_f32 v[12:13], v[192:193], s[22:23] op_sel_hi:[1,0]
	v_pk_mul_f32 v[16:17], v[196:197], s[22:23] op_sel_hi:[1,0]
	v_pk_fma_f32 v[26:27], v[104:105], s[24:25], v[14:15] op_sel_hi:[1,0,1]
	v_pk_fma_f32 v[28:29], v[102:103], s[24:25], v[12:13] op_sel_hi:[1,0,1]
	v_pk_fma_f32 v[32:33], v[94:95], s[24:25], v[16:17] op_sel_hi:[1,0,1]
	v_med3_f32 v28, v28, s74, v215
	v_med3_f32 v29, v29, s74, v215
	v_med3_f32 v90, v26, s74, v215
	v_mov_b32_e32 v26, 0
	v_med3_f32 v91, v27, s74, v215
	v_cvt_pk_fp8_f32 v26, v28, v29
	v_med3_f32 v28, v32, s74, v215
	v_med3_f32 v29, v33, s74, v215
	v_mov_b32_e32 v27, 0
	v_cvt_pk_fp8_f32 v27, v28, v29
	v_pk_mul_f32 v[18:19], v[198:199], s[22:23] op_sel_hi:[1,0]
	v_pk_fma_f32 v[82:83], v[82:83], s[24:25], v[16:17] op_sel_hi:[1,0,1]
	v_pk_fma_f32 v[30:31], v[96:97], s[24:25], v[18:19] op_sel_hi:[1,0,1]
	v_pk_fma_f32 v[32:33], v[84:85], s[24:25], v[18:19] op_sel_hi:[1,0,1]
	v_med3_f32 v28, v30, s74, v215
	v_med3_f32 v29, v31, s74, v215
	v_cvt_pk_fp8_f32 v27, v28, v29 op_sel:[0,0,1]
	v_pk_fma_f32 v[28:29], v[88:89], s[24:25], v[14:15] op_sel_hi:[1,0,1]
	v_pk_fma_f32 v[30:31], v[86:87], s[24:25], v[12:13] op_sel_hi:[1,0,1]
	v_med3_f32 v84, v28, s74, v215
	v_med3_f32 v30, v30, s74, v215
	v_med3_f32 v31, v31, s74, v215
	v_mov_b32_e32 v28, 0
	v_med3_f32 v85, v29, s74, v215
	v_cvt_pk_fp8_f32 v28, v30, v31
	v_med3_f32 v30, v82, s74, v215
	v_med3_f32 v31, v83, s74, v215
	v_mov_b32_e32 v29, 0
	v_cvt_pk_fp8_f32 v29, v30, v31
	v_med3_f32 v30, v32, s74, v215
	v_med3_f32 v31, v33, s74, v215
	v_pk_fma_f32 v[32:33], v[78:79], s[24:25], v[12:13] op_sel_hi:[1,0,1]
	v_cvt_pk_fp8_f32 v29, v30, v31 op_sel:[0,0,1]
	v_pk_fma_f32 v[30:31], v[80:81], s[24:25], v[14:15] op_sel_hi:[1,0,1]
	v_pk_fma_f32 v[74:75], v[74:75], s[24:25], v[16:17] op_sel_hi:[1,0,1]
	v_med3_f32 v32, v32, s74, v215
	v_med3_f32 v33, v33, s74, v215
	v_med3_f32 v78, v30, s74, v215
	v_mov_b32_e32 v30, 0
	v_med3_f32 v79, v31, s74, v215
	v_cvt_pk_fp8_f32 v30, v32, v33
	v_med3_f32 v32, v74, s74, v215
	v_med3_f32 v33, v75, s74, v215
	v_mov_b32_e32 v31, 0
	v_cvt_pk_fp8_f32 v31, v32, v33
	v_pk_fma_f32 v[76:77], v[76:77], s[24:25], v[18:19] op_sel_hi:[1,0,1]
	v_pk_fma_f32 v[70:71], v[70:71], s[24:25], v[12:13] op_sel_hi:[1,0,1]
	v_med3_f32 v32, v76, s74, v215
	v_med3_f32 v33, v77, s74, v215
	v_cvt_pk_fp8_f32 v31, v32, v33 op_sel:[0,0,1]
	v_pk_fma_f32 v[32:33], v[72:73], s[24:25], v[14:15] op_sel_hi:[1,0,1]
	v_pk_fma_f32 v[66:67], v[66:67], s[24:25], v[16:17] op_sel_hi:[1,0,1]
	v_med3_f32 v70, v70, s74, v215
	v_med3_f32 v71, v71, s74, v215
	v_med3_f32 v72, v32, s74, v215
	v_med3_f32 v73, v33, s74, v215
	v_mov_b32_e32 v32, 0
	v_med3_f32 v66, v66, s74, v215
	v_med3_f32 v67, v67, s74, v215
	v_mov_b32_e32 v33, 0
	v_cvt_pk_fp8_f32 v32, v70, v71
	v_cvt_pk_fp8_f32 v33, v66, v67
	v_cvt_pk_fp8_f32 v26, v90, v91 op_sel:[0,0,1]
	v_cvt_pk_fp8_f32 v28, v84, v85 op_sel:[0,0,1]
	v_pk_fma_f32 v[68:69], v[68:69], s[24:25], v[18:19] op_sel_hi:[1,0,1]
	v_cvt_pk_fp8_f32 v30, v78, v79 op_sel:[0,0,1]
	v_med3_f32 v66, v68, s74, v215
	v_med3_f32 v67, v69, s74, v215
	v_cvt_pk_fp8_f32 v32, v72, v73 op_sel:[0,0,1]
	v_cvt_pk_fp8_f32 v33, v66, v67 op_sel:[0,0,1]
	global_store_dwordx2 v[4:5], v[26:27], off offset:128
	global_store_dwordx2 v[6:7], v[28:29], off offset:128
	global_store_dwordx2 v[8:9], v[30:31], off offset:128
	global_store_dwordx2 v[10:11], v[32:33], off offset:128
	v_pk_fma_f32 v[4:5], v[64:65], s[24:25], v[14:15] op_sel_hi:[1,0,1]
	v_pk_fma_f32 v[6:7], v[62:63], s[24:25], v[12:13] op_sel_hi:[1,0,1]
	v_pk_fma_f32 v[10:11], v[58:59], s[24:25], v[16:17] op_sel_hi:[1,0,1]
	v_med3_f32 v6, v6, s74, v215
	v_med3_f32 v7, v7, s74, v215
	v_med3_f32 v26, v4, s74, v215
	v_mov_b32_e32 v4, 0
	v_med3_f32 v27, v5, s74, v215
	v_cvt_pk_fp8_f32 v4, v6, v7
	v_med3_f32 v6, v10, s74, v215
	v_med3_f32 v7, v11, s74, v215
	v_mov_b32_e32 v5, 0
	v_cvt_pk_fp8_f32 v5, v6, v7
	v_pk_fma_f32 v[8:9], v[60:61], s[24:25], v[18:19] op_sel_hi:[1,0,1]
	v_cvt_pk_fp8_f32 v4, v26, v27 op_sel:[0,0,1]
	v_med3_f32 v6, v8, s74, v215
	v_med3_f32 v7, v9, s74, v215
	v_cvt_pk_fp8_f32 v5, v6, v7 op_sel:[0,0,1]
	v_pk_fma_f32 v[6:7], v[56:57], s[24:25], v[14:15] op_sel_hi:[1,0,1]
	v_pk_fma_f32 v[8:9], v[54:55], s[24:25], v[12:13] op_sel_hi:[1,0,1]
	v_pk_fma_f32 v[26:27], v[50:51], s[24:25], v[16:17] op_sel_hi:[1,0,1]
	v_med3_f32 v8, v8, s74, v215
	v_med3_f32 v9, v9, s74, v215
	v_med3_f32 v28, v6, s74, v215
	v_mov_b32_e32 v6, 0
	v_med3_f32 v29, v7, s74, v215
	v_cvt_pk_fp8_f32 v6, v8, v9
	v_med3_f32 v8, v26, s74, v215
	v_med3_f32 v9, v27, s74, v215
	v_mov_b32_e32 v7, 0
	v_cvt_pk_fp8_f32 v7, v8, v9
	v_pk_fma_f32 v[10:11], v[52:53], s[24:25], v[18:19] op_sel_hi:[1,0,1]
	v_cvt_pk_fp8_f32 v6, v28, v29 op_sel:[0,0,1]
	v_med3_f32 v8, v10, s74, v215
	v_med3_f32 v9, v11, s74, v215
	v_cvt_pk_fp8_f32 v7, v8, v9 op_sel:[0,0,1]
	v_pk_fma_f32 v[8:9], v[48:49], s[24:25], v[14:15] op_sel_hi:[1,0,1]
	v_pk_fma_f32 v[10:11], v[46:47], s[24:25], v[12:13] op_sel_hi:[1,0,1]
	v_pk_fma_f32 v[28:29], v[42:43], s[24:25], v[16:17] op_sel_hi:[1,0,1]
	v_med3_f32 v10, v10, s74, v215
	v_med3_f32 v11, v11, s74, v215
	v_med3_f32 v30, v8, s74, v215
	v_mov_b32_e32 v8, 0
	v_med3_f32 v31, v9, s74, v215
	v_cvt_pk_fp8_f32 v8, v10, v11
	v_med3_f32 v10, v28, s74, v215
	v_med3_f32 v11, v29, s74, v215
	v_mov_b32_e32 v9, 0
	v_cvt_pk_fp8_f32 v9, v10, v11
	v_pk_fma_f32 v[26:27], v[44:45], s[24:25], v[18:19] op_sel_hi:[1,0,1]
	v_pk_fma_f32 v[12:13], v[38:39], s[24:25], v[12:13] op_sel_hi:[1,0,1]
	v_med3_f32 v10, v26, s74, v215
	v_med3_f32 v11, v27, s74, v215
	v_cvt_pk_fp8_f32 v9, v10, v11 op_sel:[0,0,1]
	v_pk_fma_f32 v[10:11], v[40:41], s[24:25], v[14:15] op_sel_hi:[1,0,1]
	v_pk_fma_f32 v[14:15], v[36:37], s[24:25], v[18:19] op_sel_hi:[1,0,1]
	v_pk_fma_f32 v[16:17], v[34:35], s[24:25], v[16:17] op_sel_hi:[1,0,1]
	v_med3_f32 v12, v12, s74, v215
	v_med3_f32 v13, v13, s74, v215
	v_med3_f32 v18, v10, s74, v215
	v_mov_b32_e32 v10, 0
	v_med3_f32 v19, v11, s74, v215
	v_cvt_pk_fp8_f32 v10, v12, v13
	v_med3_f32 v12, v16, s74, v215
	v_med3_f32 v13, v17, s74, v215
	v_mov_b32_e32 v11, 0
	v_cvt_pk_fp8_f32 v11, v12, v13
	v_cvt_pk_fp8_f32 v8, v30, v31 op_sel:[0,0,1]
	v_med3_f32 v12, v14, s74, v215
	v_med3_f32 v13, v15, s74, v215
	v_cvt_pk_fp8_f32 v10, v18, v19 op_sel:[0,0,1]
	v_cvt_pk_fp8_f32 v11, v12, v13 op_sel:[0,0,1]
	global_store_dwordx2 v[2:3], v[4:5], off offset:128
	global_store_dwordx2 v[20:21], v[6:7], off offset:128
	global_store_dwordx2 v[22:23], v[8:9], off offset:128
	global_store_dwordx2 v[24:25], v[10:11], off offset:128
	s_cbranch_vccnz .LBB0_871
	s_branch .Lp7_entry_pre
